# combo9 + P0 transposes: touch-load the tile two steps ahead (one dword per lane per tile into an unused VGPR), waits vmcnt 10..3
# baseline (speedup 1.0000x reference)
.LBB0_29:
	s_mov_b32 s1, 0
	s_mov_b32 s2, 0
	s_cmpk_gt_i32 s68, 0xbff
	s_cbranch_scc1 .LBB0_36
	v_mbcnt_lo_u32_b32 v0, -1, s2
	v_mbcnt_hi_u32_b32 v40, -1, v0
	v_readlane_b32 s2, v254, 4
	s_add_u32 s4, s48, 0x8400000
	v_readlane_b32 s3, v254, 5
	v_add_u32_e32 v37, s2, v40
	s_mul_hi_i32 s2, s68, 0x2aaaaaab
	s_addc_u32 s5, s49, 0
	s_lshr_b32 s3, s2, 31
	s_ashr_i32 s2, s2, 5
	s_add_i32 s2, s2, s3
	s_mul_i32 s3, s2, 0xc0
	s_sub_i32 s3, s68, s3
	v_ashrrev_i32_e32 v36, 4, v37
	v_lshl_add_u32 v30, s2, 8, v36
	s_lshl_b32 s2, s3, 6
	s_ashr_i32 s3, s2, 31
	s_lshl_b64 s[2:3], s[2:3], 2
	s_add_u32 s2, s24, s2
	v_lshlrev_b32_e32 v0, 4, v40
	s_addc_u32 s3, s25, s3
	v_and_b32_e32 v32, 0xf0, v0
	v_mov_b32_e32 v33, 0
	v_lshl_add_u64 v[24:25], s[2:3], 0, v[32:33]
	s_mov_b32 s2, 0xc040
	v_mad_i64_i32 v[8:9], s[6:7], v30, s2, v[24:25]
	v_add_u32_e32 v0, 32, v30
	v_mad_i64_i32 v[10:11], s[6:7], v0, s2, v[24:25]
	global_load_dwordx4 v[0:3], v[8:9], off
	global_load_dwordx4 v[4:7], v[10:11], off
	v_add_u32_e32 v8, 64, v30
	v_mad_i64_i32 v[16:17], s[6:7], v8, s2, v[24:25]
	v_add_u32_e32 v8, 0x60, v30
	v_mad_i64_i32 v[18:19], s[6:7], v8, s2, v[24:25]
	global_load_dwordx4 v[8:11], v[16:17], off
	global_load_dwordx4 v[12:15], v[18:19], off
	v_add_u32_e32 v16, 0x80, v30
	v_mad_i64_i32 v[26:27], s[6:7], v16, s2, v[24:25]
	v_add_u32_e32 v16, 0xa0, v30
	v_mad_i64_i32 v[28:29], s[6:7], v16, s2, v[24:25]
	global_load_dwordx4 v[16:19], v[26:27], off
	global_load_dwordx4 v[20:23], v[28:29], off
	v_add_u32_e32 v26, 0xc0, v30
	v_mad_i64_i32 v[34:35], s[6:7], v26, s2, v[24:25]
	v_add_u32_e32 v26, 0xe0, v30
	v_mad_i64_i32 v[38:39], s[6:7], v26, s2, v[24:25]
	global_load_dwordx4 v[24:27], v[34:35], off
	global_load_dwordx4 v[28:31], v[38:39], off
	v_add_u32_e32 v39, 0, v32
	v_lshl_add_u64 v[34:35], s[24:25], 0, v[32:33]
	v_lshlrev_b32_e32 v32, 5, v40
	v_ashrrev_i32_e32 v37, 3, v37
	v_and_b32_e32 v32, 0xe0, v32
	s_movk_i32 s3, 0x104
	v_mul_u32_u24_e32 v38, 0x104, v32
	v_lshlrev_b32_e32 v40, 2, v37
	v_add3_u32 v38, 0, v38, v40
	v_mul_lo_u32 v40, v36, s3
	v_add_u32_e32 v39, v39, v40
	s_lshl_b32 s10, s68, 6
	s_lshl_b32 s3, s46, 6
	v_add_u32_e32 v40, 0x2080, v39
	v_add_u32_e32 v41, 0x2088, v39
	v_add_u32_e32 v42, 0x4100, v39
	v_add_u32_e32 v43, 0x4108, v39
	v_add_u32_e32 v44, 0x6180, v39
	v_add_u32_e32 v45, 0x6188, v39
	v_add_u32_e32 v46, 0x8200, v39
	v_add_u32_e32 v47, 0x8208, v39
	v_add_u32_e32 v48, 0xa280, v39
	v_add_u32_e32 v49, 0xa288, v39
	v_add_u32_e32 v50, 0xc300, v39
	v_add_u32_e32 v51, 0xc308, v39
	v_add_u32_e32 v52, 0xe380, v39
	s_mov_b32 s31, s68
	global_load_dword v200, v[34:35], off
	global_load_dword v200, v[34:35], off
	global_load_dword v200, v[34:35], off
	v_mbcnt_lo_u32_b32 v201, -1, 0
	v_mbcnt_hi_u32_b32 v201, -1, v201
	v_readlane_b32 s72, v254, 4
	v_add_u32_e32 v201, s72, v201
	v_lshrrev_b32_e32 v204, 1, v201
	v_mul_u32_u24_e32 v204, 0xc040, v204
	v_and_b32_e32 v205, 1, v201
	v_lshl_add_u32 v204, v205, 7, v204
	v_and_b32_e32 v205, 15, v201
	v_lshlrev_b32_e32 v205, 4, v205
	v_sub_u32_e32 v204, v204, v205
	v_mov_b32_e32 v205, 0
	v_lshl_add_u64 v[202:203], v[204:205], 0, v[34:35]
	s_branch .LBB0_32

.LBB0_32:
	s_add_i32 s11, s31, s46
	s_cmpk_gt_i32 s11, 0xbff
	v_add_u32_e32 v53, 0xe388, v39
	s_cselect_b64 s[6:7], -1, 0
	s_cmpk_lt_i32 s11, 0xc00
	s_mov_b64 s[8:9], -1
	s_waitcnt vmcnt(10)
	ds_write2_b32 v39, v0, v1 offset1:1
	ds_write2_b32 v39, v2, v3 offset0:2 offset1:3
	s_waitcnt vmcnt(9)
	ds_write2_b32 v40, v4, v5 offset1:1
	ds_write2_b32 v41, v6, v7 offset1:1
	s_waitcnt vmcnt(8)
	ds_write2_b32 v42, v8, v9 offset1:1
	ds_write2_b32 v43, v10, v11 offset1:1
	s_waitcnt vmcnt(7)
	ds_write2_b32 v44, v12, v13 offset1:1
	ds_write2_b32 v45, v14, v15 offset1:1
	s_waitcnt vmcnt(6)
	ds_write2_b32 v46, v16, v17 offset1:1
	ds_write2_b32 v47, v18, v19 offset1:1
	s_waitcnt vmcnt(5)
	ds_write2_b32 v48, v20, v21 offset1:1
	ds_write2_b32 v49, v22, v23 offset1:1
	s_waitcnt vmcnt(4)
	ds_write2_b32 v50, v24, v25 offset1:1
	ds_write2_b32 v51, v26, v27 offset1:1
	s_waitcnt vmcnt(3)
	ds_write2_b32 v52, v28, v29 offset1:1
	ds_write2_b32 v53, v30, v31 offset1:1
	s_waitcnt lgkmcnt(0)
	s_barrier
	s_cbranch_scc1 .LBB0_34
	s_add_i32 s30, s10, s3
	s_mov_b64 s[8:9], 0
.LBB0_34:
	s_andn2_b64 vcc, exec, s[8:9]
	s_cbranch_vccnz .LBB0_31
	s_mul_hi_i32 s8, s11, 0x2aaaaaab
	s_lshr_b32 s9, s8, 31
	s_ashr_i32 s8, s8, 5
	s_add_i32 s8, s8, s9
	v_lshl_add_u32 v30, s8, 8, v36
	s_mulk_i32 s8, 0xd000
	s_add_i32 s30, s3, s10
	s_add_i32 s8, s30, s8
	s_ashr_i32 s9, s8, 31
	v_lshl_add_u64 v[24:25], s[8:9], 2, v[34:35]
	v_mad_i64_i32 v[8:9], s[8:9], v30, s2, v[24:25]
	v_add_u32_e32 v0, 32, v30
	v_mad_i64_i32 v[10:11], s[8:9], v0, s2, v[24:25]
	global_load_dwordx4 v[0:3], v[8:9], off
	global_load_dwordx4 v[4:7], v[10:11], off
	v_add_u32_e32 v8, 64, v30
	v_mad_i64_i32 v[16:17], s[8:9], v8, s2, v[24:25]
	v_add_u32_e32 v8, 0x60, v30
	v_mad_i64_i32 v[18:19], s[8:9], v8, s2, v[24:25]
	global_load_dwordx4 v[8:11], v[16:17], off
	global_load_dwordx4 v[12:15], v[18:19], off
	v_add_u32_e32 v16, 0x80, v30
	v_mad_i64_i32 v[26:27], s[8:9], v16, s2, v[24:25]
	v_add_u32_e32 v16, 0xa0, v30
	v_mad_i64_i32 v[28:29], s[8:9], v16, s2, v[24:25]
	global_load_dwordx4 v[16:19], v[26:27], off
	global_load_dwordx4 v[20:23], v[28:29], off
	v_add_u32_e32 v26, 0xc0, v30
	v_mad_i64_i32 v[54:55], s[8:9], v26, s2, v[24:25]
	v_add_u32_e32 v26, 0xe0, v30
	v_mad_i64_i32 v[56:57], s[8:9], v26, s2, v[24:25]
	global_load_dwordx4 v[24:27], v[54:55], off
	global_load_dwordx4 v[28:31], v[56:57], off
	s_add_i32 s72, s11, s46
	s_cmp_lt_i32 s72, 0xc00
	s_cselect_b32 s72, s72, s11
	s_lshr_b32 s73, s72, 6
	s_mul_i32 s73, s73, 43
	s_lshr_b32 s73, s73, 7
	s_mul_i32 s74, s73, 0xc0
	s_sub_i32 s72, s72, s74
	s_mul_i32 s73, s73, 0xc04000
	s_lshl_b32 s72, s72, 8
	s_add_u32 s72, s72, s73
	s_mov_b32 s73, 0
	v_lshl_add_u64 v[206:207], v[202:203], 0, s[72:73]
	global_load_dword v200, v[206:207], off
	s_branch .LBB0_31
.LBB0_36:
	s_cmpk_lt_i32 s68, 0x400
	s_cselect_b64 s[4:5], -1, 0
	s_cmpk_gt_i32 s68, 0x3ff
	s_cbranch_scc1 .LBB0_43
	s_add_u32 s6, s48, 0xe400000
	s_addc_u32 s7, s49, 0
	s_waitcnt vmcnt(9)
	v_mbcnt_lo_u32_b32 v0, -1, s1
	s_ashr_i32 s1, s68, 31
	s_lshr_b32 s1, s1, 26
	v_mbcnt_hi_u32_b32 v40, -1, v0
	v_readlane_b32 s2, v254, 4
	s_add_i32 s1, s68, s1
	v_readlane_b32 s3, v254, 5
	v_add_u32_e32 v37, s2, v40
	s_and_b32 s2, s1, 0x3ffffc0
	s_sub_i32 s2, s68, s2
	s_lshl_b32 s2, s2, 6
	s_lshl_b32 s1, s1, 2
	s_ashr_i32 s3, s2, 31
	v_ashrrev_i32_e32 v36, 4, v37
	s_and_b32 s1, s1, 0xffffff00
	s_lshl_b64 s[2:3], s[2:3], 2
	s_waitcnt vmcnt(3)
	v_add_u32_e32 v24, s1, v36
	s_add_u32 s2, s28, s2
	v_lshlrev_b32_e32 v0, 4, v40
	s_addc_u32 s3, s29, s3
	v_and_b32_e32 v32, 0xf0, v0
	v_mov_b32_e32 v33, 0
	v_ashrrev_i32_e32 v25, 31, v24
	v_lshl_add_u64 v[26:27], s[2:3], 0, v[32:33]
	v_lshlrev_b64 v[0:1], 14, v[24:25]
	v_lshl_add_u64 v[8:9], v[26:27], 0, v[0:1]
	v_add_u32_e32 v0, 32, v24
	v_ashrrev_i32_e32 v1, 31, v0
	v_lshlrev_b64 v[0:1], 14, v[0:1]
	v_lshl_add_u64 v[10:11], v[26:27], 0, v[0:1]
	global_load_dwordx4 v[0:3], v[8:9], off
	global_load_dwordx4 v[4:7], v[10:11], off
	v_add_u32_e32 v8, 64, v24
	v_ashrrev_i32_e32 v9, 31, v8
	v_lshlrev_b64 v[8:9], 14, v[8:9]
	v_lshl_add_u64 v[16:17], v[26:27], 0, v[8:9]
	v_add_u32_e32 v8, 0x60, v24
	v_ashrrev_i32_e32 v9, 31, v8
	v_lshlrev_b64 v[8:9], 14, v[8:9]
	v_lshl_add_u64 v[18:19], v[26:27], 0, v[8:9]
	global_load_dwordx4 v[8:11], v[16:17], off
	global_load_dwordx4 v[12:15], v[18:19], off
	v_add_u32_e32 v16, 0x80, v24
	v_ashrrev_i32_e32 v17, 31, v16
	v_lshlrev_b64 v[16:17], 14, v[16:17]
	s_waitcnt vmcnt(6)
	v_lshl_add_u64 v[28:29], v[26:27], 0, v[16:17]
	v_add_u32_e32 v16, 0xa0, v24
	v_ashrrev_i32_e32 v17, 31, v16
	v_lshlrev_b64 v[16:17], 14, v[16:17]
	v_lshl_add_u64 v[30:31], v[26:27], 0, v[16:17]
	global_load_dwordx4 v[16:19], v[28:29], off
	global_load_dwordx4 v[20:23], v[30:31], off
	v_add_u32_e32 v28, 0xc0, v24
	v_ashrrev_i32_e32 v29, 31, v28
	v_add_u32_e32 v24, 0xe0, v24
	v_lshlrev_b64 v[28:29], 14, v[28:29]
	v_ashrrev_i32_e32 v25, 31, v24
	v_lshl_add_u64 v[34:35], v[26:27], 0, v[28:29]
	v_lshlrev_b64 v[24:25], 14, v[24:25]
	v_lshl_add_u64 v[38:39], v[26:27], 0, v[24:25]
	global_load_dwordx4 v[24:27], v[34:35], off
	global_load_dwordx4 v[28:31], v[38:39], off
	v_add_u32_e32 v39, 0, v32
	v_lshl_add_u64 v[34:35], s[28:29], 0, v[32:33]
	v_lshlrev_b32_e32 v32, 5, v40
	v_ashrrev_i32_e32 v37, 3, v37
	v_and_b32_e32 v32, 0xe0, v32
	s_movk_i32 s1, 0x104
	v_mul_u32_u24_e32 v38, 0x104, v32
	v_lshlrev_b32_e32 v40, 2, v37
	v_add3_u32 v38, 0, v38, v40
	v_mul_lo_u32 v40, v36, s1
	s_lshl_b32 s2, s68, 6
	s_lshl_b32 s1, s46, 6
	v_add_u32_e32 v39, v39, v40
	s_mov_b32 s29, s68
	global_load_dword v200, v[34:35], off
	global_load_dword v200, v[34:35], off
	global_load_dword v200, v[34:35], off
	v_mbcnt_lo_u32_b32 v201, -1, 0
	v_mbcnt_hi_u32_b32 v201, -1, v201
	v_readlane_b32 s72, v254, 4
	v_add_u32_e32 v201, s72, v201
	v_lshrrev_b32_e32 v204, 1, v201
	v_mul_u32_u24_e32 v204, 0x4000, v204
	v_and_b32_e32 v205, 1, v201
	v_lshl_add_u32 v204, v205, 7, v204
	v_and_b32_e32 v205, 15, v201
	v_lshlrev_b32_e32 v205, 4, v205
	v_sub_u32_e32 v204, v204, v205
	v_mov_b32_e32 v205, 0
	v_lshl_add_u64 v[202:203], v[204:205], 0, v[34:35]
	s_branch .LBB0_39

.LBB0_39:
	v_add_u32_e32 v40, 0x2080, v39
	s_waitcnt vmcnt(10)
	ds_write2_b32 v39, v0, v1 offset1:1
	ds_write2_b32 v39, v2, v3 offset0:2 offset1:3
	s_waitcnt vmcnt(9)
	ds_write2_b32 v40, v4, v5 offset1:1
	v_add_u32_e32 v40, 0x2088, v39
	ds_write2_b32 v40, v6, v7 offset1:1
	v_add_u32_e32 v40, 0x4100, v39
	s_waitcnt vmcnt(8)
	ds_write2_b32 v40, v8, v9 offset1:1
	v_add_u32_e32 v40, 0x4108, v39
	ds_write2_b32 v40, v10, v11 offset1:1
	v_add_u32_e32 v40, 0x6180, v39
	s_waitcnt vmcnt(7)
	ds_write2_b32 v40, v12, v13 offset1:1
	v_add_u32_e32 v40, 0x6188, v39
	ds_write2_b32 v40, v14, v15 offset1:1
	v_add_u32_e32 v40, 0x8200, v39
	s_waitcnt vmcnt(6)
	ds_write2_b32 v40, v16, v17 offset1:1
	v_add_u32_e32 v40, 0x8208, v39
	ds_write2_b32 v40, v18, v19 offset1:1
	v_add_u32_e32 v40, 0xa280, v39
	s_waitcnt vmcnt(5)
	ds_write2_b32 v40, v20, v21 offset1:1
	v_add_u32_e32 v40, 0xa288, v39
	ds_write2_b32 v40, v22, v23 offset1:1
	v_add_u32_e32 v40, 0xc300, v39
	s_waitcnt vmcnt(4)
	ds_write2_b32 v40, v24, v25 offset1:1
	v_add_u32_e32 v40, 0xc308, v39
	s_add_i32 s3, s29, s46
	ds_write2_b32 v40, v26, v27 offset1:1
	v_add_u32_e32 v40, 0xe380, v39
	s_cmpk_gt_i32 s3, 0x3ff
	s_waitcnt vmcnt(3)
	ds_write2_b32 v40, v28, v29 offset1:1
	v_add_u32_e32 v40, 0xe388, v39
	s_cselect_b64 s[8:9], -1, 0
	s_cmpk_lt_i32 s3, 0x400
	s_mov_b64 s[10:11], -1
	ds_write2_b32 v40, v30, v31 offset1:1
	s_waitcnt lgkmcnt(0)
	s_barrier
	s_cbranch_scc1 .LBB0_41
	s_add_i32 s28, s2, s1
	s_mov_b64 s[10:11], 0
.LBB0_41:
	s_andn2_b64 vcc, exec, s[10:11]
	s_cbranch_vccnz .LBB0_38
	s_ashr_i32 s10, s3, 31
	s_lshr_b32 s10, s10, 26
	s_add_i32 s10, s3, s10
	s_ashr_i32 s10, s10, 6
	v_lshl_add_u32 v24, s10, 8, v36
	s_add_i32 s28, s1, s2
	s_lshl_b32 s10, s10, 12
	s_sub_i32 s10, s28, s10
	s_ashr_i32 s11, s10, 31
	v_ashrrev_i32_e32 v25, 31, v24
	v_lshl_add_u64 v[26:27], s[10:11], 2, v[34:35]
	v_lshlrev_b64 v[0:1], 14, v[24:25]
	v_lshl_add_u64 v[8:9], v[26:27], 0, v[0:1]
	v_add_u32_e32 v0, 32, v24
	v_ashrrev_i32_e32 v1, 31, v0
	v_lshlrev_b64 v[0:1], 14, v[0:1]
	v_lshl_add_u64 v[10:11], v[26:27], 0, v[0:1]
	global_load_dwordx4 v[0:3], v[8:9], off
	global_load_dwordx4 v[4:7], v[10:11], off
	v_add_u32_e32 v8, 64, v24
	v_ashrrev_i32_e32 v9, 31, v8
	v_lshlrev_b64 v[8:9], 14, v[8:9]
	v_lshl_add_u64 v[16:17], v[26:27], 0, v[8:9]
	v_add_u32_e32 v8, 0x60, v24
	v_ashrrev_i32_e32 v9, 31, v8
	v_lshlrev_b64 v[8:9], 14, v[8:9]
	v_lshl_add_u64 v[18:19], v[26:27], 0, v[8:9]
	global_load_dwordx4 v[8:11], v[16:17], off
	global_load_dwordx4 v[12:15], v[18:19], off
	v_add_u32_e32 v16, 0x80, v24
	v_ashrrev_i32_e32 v17, 31, v16
	v_lshlrev_b64 v[16:17], 14, v[16:17]
	v_lshl_add_u64 v[28:29], v[26:27], 0, v[16:17]
	v_add_u32_e32 v16, 0xa0, v24
	v_ashrrev_i32_e32 v17, 31, v16
	v_lshlrev_b64 v[16:17], 14, v[16:17]
	v_lshl_add_u64 v[30:31], v[26:27], 0, v[16:17]
	global_load_dwordx4 v[16:19], v[28:29], off
	global_load_dwordx4 v[20:23], v[30:31], off
	v_add_u32_e32 v28, 0xc0, v24
	v_ashrrev_i32_e32 v29, 31, v28
	v_add_u32_e32 v24, 0xe0, v24
	v_lshlrev_b64 v[28:29], 14, v[28:29]
	v_ashrrev_i32_e32 v25, 31, v24
	v_lshl_add_u64 v[40:41], v[26:27], 0, v[28:29]
	v_lshlrev_b64 v[24:25], 14, v[24:25]
	v_lshl_add_u64 v[42:43], v[26:27], 0, v[24:25]
	global_load_dwordx4 v[24:27], v[40:41], off
	global_load_dwordx4 v[28:31], v[42:43], off
	s_add_i32 s72, s3, s46
	s_cmp_lt_i32 s72, 0x400
	s_cselect_b32 s72, s72, s3
	s_lshr_b32 s73, s72, 6
	s_and_b32 s72, s72, 63
	s_mul_i32 s73, s73, 0x400000
	s_lshl_b32 s72, s72, 8
	s_add_u32 s72, s72, s73
	s_mov_b32 s73, 0
	v_lshl_add_u64 v[206:207], v[202:203], 0, s[72:73]
	global_load_dword v200, v[206:207], off
	s_branch .LBB0_38
.LBB0_43:
	s_mov_b32 s1, 0
	s_mov_b32 s2, 0
	s_cmpk_gt_i32 s68, 0xfff
	s_cbranch_scc1 .LBB0_50
	s_waitcnt vmcnt(9)
	v_mbcnt_lo_u32_b32 v0, -1, s2
	s_add_u32 s6, s48, 0x19400000
	v_mbcnt_hi_u32_b32 v40, -1, v0
	v_readlane_b32 s2, v254, 4
	s_addc_u32 s7, s49, 0
	v_readlane_b32 s3, v254, 5
	v_add_u32_e32 v37, s2, v40
	s_ashr_i32 s2, s68, 31
	s_lshr_b32 s2, s2, 26
	s_add_i32 s2, s68, s2
	s_and_b32 s3, s2, 0x3ffffc0
	s_lshl_b32 s2, s2, 2
	s_sub_i32 s3, s68, s3
	v_ashrrev_i32_e32 v36, 4, v37
	s_and_b32 s2, s2, 0xffffff00
	s_waitcnt vmcnt(3)
	v_add_u32_e32 v24, s2, v36
	s_lshl_b32 s2, s3, 6
	s_ashr_i32 s3, s2, 31
	s_lshl_b64 s[2:3], s[2:3], 2
	s_add_u32 s2, s26, s2
	v_lshlrev_b32_e32 v0, 4, v40
	s_addc_u32 s3, s27, s3
	v_and_b32_e32 v32, 0xf0, v0
	v_mov_b32_e32 v33, 0
	v_ashrrev_i32_e32 v25, 31, v24
	v_lshl_add_u64 v[26:27], s[2:3], 0, v[32:33]
	v_lshlrev_b64 v[0:1], 14, v[24:25]
	v_lshl_add_u64 v[8:9], v[26:27], 0, v[0:1]
	v_add_u32_e32 v0, 32, v24
	v_ashrrev_i32_e32 v1, 31, v0
	v_lshlrev_b64 v[0:1], 14, v[0:1]
	v_lshl_add_u64 v[10:11], v[26:27], 0, v[0:1]
	global_load_dwordx4 v[0:3], v[8:9], off
	global_load_dwordx4 v[4:7], v[10:11], off
	v_add_u32_e32 v8, 64, v24
	v_ashrrev_i32_e32 v9, 31, v8
	v_lshlrev_b64 v[8:9], 14, v[8:9]
	v_lshl_add_u64 v[16:17], v[26:27], 0, v[8:9]
	v_add_u32_e32 v8, 0x60, v24
	v_ashrrev_i32_e32 v9, 31, v8
	v_lshlrev_b64 v[8:9], 14, v[8:9]
	v_lshl_add_u64 v[18:19], v[26:27], 0, v[8:9]
	global_load_dwordx4 v[8:11], v[16:17], off
	global_load_dwordx4 v[12:15], v[18:19], off
	v_add_u32_e32 v16, 0x80, v24
	v_ashrrev_i32_e32 v17, 31, v16
	v_lshlrev_b64 v[16:17], 14, v[16:17]
	s_waitcnt vmcnt(6)
	v_lshl_add_u64 v[28:29], v[26:27], 0, v[16:17]
	v_add_u32_e32 v16, 0xa0, v24
	v_ashrrev_i32_e32 v17, 31, v16
	v_lshlrev_b64 v[16:17], 14, v[16:17]
	v_lshl_add_u64 v[30:31], v[26:27], 0, v[16:17]
	global_load_dwordx4 v[16:19], v[28:29], off
	global_load_dwordx4 v[20:23], v[30:31], off
	v_add_u32_e32 v28, 0xc0, v24
	v_ashrrev_i32_e32 v29, 31, v28
	v_add_u32_e32 v24, 0xe0, v24
	v_lshlrev_b64 v[28:29], 14, v[28:29]
	v_ashrrev_i32_e32 v25, 31, v24
	v_lshl_add_u64 v[34:35], v[26:27], 0, v[28:29]
	v_lshlrev_b64 v[24:25], 14, v[24:25]
	v_lshl_add_u64 v[38:39], v[26:27], 0, v[24:25]
	global_load_dwordx4 v[24:27], v[34:35], off
	global_load_dwordx4 v[28:31], v[38:39], off
	v_add_u32_e32 v39, 0, v32
	v_lshl_add_u64 v[34:35], s[26:27], 0, v[32:33]
	v_lshlrev_b32_e32 v32, 5, v40
	v_ashrrev_i32_e32 v37, 3, v37
	v_and_b32_e32 v32, 0xe0, v32
	s_movk_i32 s2, 0x104
	v_mul_u32_u24_e32 v38, 0x104, v32
	v_lshlrev_b32_e32 v40, 2, v37
	v_add3_u32 v38, 0, v38, v40
	v_mul_lo_u32 v40, v36, s2
	s_lshl_b32 s3, s68, 6
	s_lshl_b32 s2, s46, 6
	v_add_u32_e32 v39, v39, v40
	s_mov_b32 s28, s68
	global_load_dword v200, v[34:35], off
	global_load_dword v200, v[34:35], off
	global_load_dword v200, v[34:35], off
	v_mbcnt_lo_u32_b32 v201, -1, 0
	v_mbcnt_hi_u32_b32 v201, -1, v201
	v_readlane_b32 s72, v254, 4
	v_add_u32_e32 v201, s72, v201
	v_lshrrev_b32_e32 v204, 1, v201
	v_mul_u32_u24_e32 v204, 0x4000, v204
	v_and_b32_e32 v205, 1, v201
	v_lshl_add_u32 v204, v205, 7, v204
	v_and_b32_e32 v205, 15, v201
	v_lshlrev_b32_e32 v205, 4, v205
	v_sub_u32_e32 v204, v204, v205
	v_mov_b32_e32 v205, 0
	v_lshl_add_u64 v[202:203], v[204:205], 0, v[34:35]
	s_branch .LBB0_46

.LBB0_46:
	v_add_u32_e32 v40, 0x2080, v39
	s_waitcnt vmcnt(10)
	ds_write2_b32 v39, v0, v1 offset1:1
	ds_write2_b32 v39, v2, v3 offset0:2 offset1:3
	s_waitcnt vmcnt(9)
	ds_write2_b32 v40, v4, v5 offset1:1
	v_add_u32_e32 v40, 0x2088, v39
	ds_write2_b32 v40, v6, v7 offset1:1
	v_add_u32_e32 v40, 0x4100, v39
	s_waitcnt vmcnt(8)
	ds_write2_b32 v40, v8, v9 offset1:1
	v_add_u32_e32 v40, 0x4108, v39
	ds_write2_b32 v40, v10, v11 offset1:1
	v_add_u32_e32 v40, 0x6180, v39
	s_waitcnt vmcnt(7)
	ds_write2_b32 v40, v12, v13 offset1:1
	v_add_u32_e32 v40, 0x6188, v39
	ds_write2_b32 v40, v14, v15 offset1:1
	v_add_u32_e32 v40, 0x8200, v39
	s_waitcnt vmcnt(6)
	ds_write2_b32 v40, v16, v17 offset1:1
	v_add_u32_e32 v40, 0x8208, v39
	ds_write2_b32 v40, v18, v19 offset1:1
	v_add_u32_e32 v40, 0xa280, v39
	s_waitcnt vmcnt(5)
	ds_write2_b32 v40, v20, v21 offset1:1
	v_add_u32_e32 v40, 0xa288, v39
	ds_write2_b32 v40, v22, v23 offset1:1
	v_add_u32_e32 v40, 0xc300, v39
	s_waitcnt vmcnt(4)
	ds_write2_b32 v40, v24, v25 offset1:1
	v_add_u32_e32 v40, 0xc308, v39
	s_add_i32 s26, s28, s46
	ds_write2_b32 v40, v26, v27 offset1:1
	v_add_u32_e32 v40, 0xe380, v39
	s_cmpk_gt_i32 s26, 0xfff
	s_waitcnt vmcnt(3)
	ds_write2_b32 v40, v28, v29 offset1:1
	v_add_u32_e32 v40, 0xe388, v39
	s_cselect_b64 s[8:9], -1, 0
	s_cmpk_lt_i32 s26, 0x1000
	s_mov_b64 s[10:11], -1
	ds_write2_b32 v40, v30, v31 offset1:1
	s_waitcnt lgkmcnt(0)
	s_barrier
	s_cbranch_scc1 .LBB0_48
	s_add_i32 s27, s3, s2
	s_mov_b64 s[10:11], 0
.LBB0_48:
	s_andn2_b64 vcc, exec, s[10:11]
	s_cbranch_vccnz .LBB0_45
	s_ashr_i32 s10, s26, 31
	s_lshr_b32 s10, s10, 26
	s_add_i32 s10, s26, s10
	s_ashr_i32 s10, s10, 6
	v_lshl_add_u32 v24, s10, 8, v36
	s_add_i32 s27, s2, s3
	s_lshl_b32 s10, s10, 12
	s_sub_i32 s10, s27, s10
	s_ashr_i32 s11, s10, 31
	v_ashrrev_i32_e32 v25, 31, v24
	v_lshl_add_u64 v[26:27], s[10:11], 2, v[34:35]
	v_lshlrev_b64 v[0:1], 14, v[24:25]
	v_lshl_add_u64 v[8:9], v[26:27], 0, v[0:1]
	v_add_u32_e32 v0, 32, v24
	v_ashrrev_i32_e32 v1, 31, v0
	v_lshlrev_b64 v[0:1], 14, v[0:1]
	v_lshl_add_u64 v[10:11], v[26:27], 0, v[0:1]
	global_load_dwordx4 v[0:3], v[8:9], off
	global_load_dwordx4 v[4:7], v[10:11], off
	v_add_u32_e32 v8, 64, v24
	v_ashrrev_i32_e32 v9, 31, v8
	v_lshlrev_b64 v[8:9], 14, v[8:9]
	v_lshl_add_u64 v[16:17], v[26:27], 0, v[8:9]
	v_add_u32_e32 v8, 0x60, v24
	v_ashrrev_i32_e32 v9, 31, v8
	v_lshlrev_b64 v[8:9], 14, v[8:9]
	v_lshl_add_u64 v[18:19], v[26:27], 0, v[8:9]
	global_load_dwordx4 v[8:11], v[16:17], off
	global_load_dwordx4 v[12:15], v[18:19], off
	v_add_u32_e32 v16, 0x80, v24
	v_ashrrev_i32_e32 v17, 31, v16
	v_lshlrev_b64 v[16:17], 14, v[16:17]
	v_lshl_add_u64 v[28:29], v[26:27], 0, v[16:17]
	v_add_u32_e32 v16, 0xa0, v24
	v_ashrrev_i32_e32 v17, 31, v16
	v_lshlrev_b64 v[16:17], 14, v[16:17]
	v_lshl_add_u64 v[30:31], v[26:27], 0, v[16:17]
	global_load_dwordx4 v[16:19], v[28:29], off
	global_load_dwordx4 v[20:23], v[30:31], off
	v_add_u32_e32 v28, 0xc0, v24
	v_ashrrev_i32_e32 v29, 31, v28
	v_add_u32_e32 v24, 0xe0, v24
	v_lshlrev_b64 v[28:29], 14, v[28:29]
	v_ashrrev_i32_e32 v25, 31, v24
	v_lshl_add_u64 v[40:41], v[26:27], 0, v[28:29]
	v_lshlrev_b64 v[24:25], 14, v[24:25]
	v_lshl_add_u64 v[42:43], v[26:27], 0, v[24:25]
	global_load_dwordx4 v[24:27], v[40:41], off
	global_load_dwordx4 v[28:31], v[42:43], off
	s_add_i32 s72, s26, s46
	s_cmp_lt_i32 s72, 0x1000
	s_cselect_b32 s72, s72, s26
	s_lshr_b32 s73, s72, 6
	s_and_b32 s72, s72, 63
	s_mul_i32 s73, s73, 0x400000
	s_lshl_b32 s72, s72, 8
	s_add_u32 s72, s72, s73
	s_mov_b32 s73, 0
	v_lshl_add_u64 v[206:207], v[202:203], 0, s[72:73]
	global_load_dword v200, v[206:207], off
	s_branch .LBB0_45
